# v92 + MLA unit prologue: redundant full vmcnt drain before the counted waits of the second K/V tile removed
# speedup vs baseline: 1.0030x; 1.0030x over previous
; #define VM_WAIT() asm volatile("s_waitcnt vmcnt(0)" ::: "memory")
; #define A_SWRITE(bf) do { *(bf16x8*)(K_lds + (bf) * SHM_K + kws) = st_k0; *(bf16x8*)(K_lds + (bf) * SHM_K + kws + 32 * ROWB) = st_k1; \
;         if constexpr (DQK == 192) *(bf16x8*)(K_lds + (bf) * SHM_K + kws2) = st_k2; \
;         *(bf16x8*)(V_lds + (bf) * SHM_V + vst0) = st_v0; *(bf16x8*)(V_lds + (bf) * SHM_V + vst1) = st_v1; } while (0)
; #define A_BAR() do { asm volatile("s_waitcnt lgkmcnt(0)" ::: "memory"); __builtin_amdgcn_s_barrier(); asm volatile("" ::: "memory"); } while (0)
; template <int DQK, bool BIAS> ...
;     ...
;     A_SLOAD(kb0); VM_WAIT(); A_SWRITE(0);
;     if (NT > 1) { A_SLOAD(kb0 + 64); VM_WAIT(); A_SWRITE(1); }
;     __syncthreads();
;     if (wid >= 4) A_BAR();
; __device__ __forceinline__ void p4_mla_loop(Frame& F, const Args& A, const int qo) {
;     ...
;         __syncthreads();
;         if (tid == 0) F.MISC[16] = __hip_atomic_fetch_add(F.ctl + CW_QUEUE + qo, 1u, RLX_AGENT);
;         __syncthreads();
;         const int it = __builtin_amdgcn_readfirstlane((int)F.MISC[16]);
;         if (it >= 512) break;
;         int ln = lane; asm volatile("" : "+v"(ln)); const int r32 = ln & 31, hi = ln >> 5;
;         const int qb = 31 - (it >> 4), bh = it & 15, b = bh >> 3, h = bh & 7;
;         const int m0 = b * SEQ + qb * 256 + wid * 32;
;         bf16x8 qr[12];
;         { const bf16_t* qp = WSP(bf16_t, WS_QF) + (size_t)(m0 + r32) * QFW + h * 192 + hi * 8;
; #pragma unroll
;           for (int d0 = 0; d0 < 12; ++d0) qr[d0] = *(const bf16x8*)(qp + d0 * 16); }
.LBB0_790:
	s_or_b64 exec, exec, s[4:5]
	s_waitcnt lgkmcnt(0)
	s_barrier
	ds_read_b32 v2, v191
	s_mov_b64 s[4:5], -1
	s_waitcnt lgkmcnt(0)
	v_readfirstlane_b32 s6, v2
	s_cmpk_lt_i32 s6, 0x200
	s_cbranch_scc0 .LBB0_785
	s_ashr_i32 s5, s6, 4
	s_lshl_b32 s4, s6, 10
	s_and_b32 s83, s6, 7
	s_and_b32 s8, s4, 0x2000
	s_lshl_b32 s4, s5, 8
	v_readlane_b32 s6, v254, 38
	s_sub_i32 s84, s6, s4
	v_mov_b32_e32 v200, v170
	s_addk_i32 s84, 0x1f00
	s_add_i32 s74, s84, s8
	v_and_b32_e32 v202, 31, v200
	v_or_b32_e32 v2, s74, v202
	v_mov_b64_e32 v[4:5], s[70:71]
	s_movk_i32 s6, 0xc00
	v_mad_i64_i32 v[4:5], s[6:7], v2, s6, v[4:5]
	s_lshl_b32 s6, s8, 12
	v_readlane_b32 s7, v255, 18
	s_add_u32 s6, s7, s6
	v_readlane_b32 s7, v255, 15
	v_ashrrev_i32_e32 v201, 5, v200
	s_addc_u32 s7, s7, 0
	s_lshl_b32 s9, s83, 9
	s_mul_i32 s68, s83, 0x180
	v_lshlrev_b32_e32 v6, 3, v201
	s_add_u32 s76, s6, s9
	v_lshl_add_u64 v[4:5], v[4:5], 0, s[68:69]
	v_ashrrev_i32_e32 v7, 31, v6
	s_addc_u32 s77, s7, 0
	s_lshl_b32 s6, s8, 7
	v_readlane_b32 s7, v255, 20
	v_lshl_add_u64 v[20:21], v[6:7], 1, v[4:5]
	s_add_u32 s6, s7, s6
	v_readlane_b32 s7, v255, 19
	v_lshl_add_u64 v[24:25], s[76:77], 0, v[174:175]
	global_load_dwordx4 v[154:157], v[20:21], off offset:32
	global_load_dwordx4 v[150:153], v[20:21], off offset:64
	global_load_dwordx4 v[142:145], v[20:21], off offset:96
	global_load_dwordx4 v[138:141], v[20:21], off offset:128
	global_load_dwordx4 v[134:137], v[20:21], off offset:160
	global_load_dwordx4 v[130:133], v[20:21], off offset:192
	global_load_dwordx4 v[126:129], v[20:21], off offset:224
	global_load_dwordx4 v[122:125], v[20:21], off offset:256
	global_load_dwordx4 v[118:121], v[20:21], off offset:288
	global_load_dwordx4 v[114:117], v[20:21], off offset:320
	s_addc_u32 s7, s7, 0
	v_add_co_u32_e32 v16, vcc, s96, v24
	v_lshl_add_u64 v[178:179], s[6:7], 0, v[176:177]
	s_nop 0
	v_addc_co_u32_e32 v17, vcc, 0, v25, vcc
	s_mov_b32 s6, 0x40000
	v_add_co_u32_e32 v36, vcc, s6, v24
	s_mov_b32 s6, 0x60000
	s_nop 0
	v_addc_co_u32_e32 v37, vcc, 0, v25, vcc
	global_load_dwordx4 v[4:7], v[16:17], off offset:256
	global_load_dwordx4 v[146:149], v[20:21], off offset:352
	global_load_dwordx4 v[8:11], v[24:25], off
	global_load_dwordx4 v[12:15], v[24:25], off offset:256
	s_nop 0
	global_load_dwordx4 v[16:19], v[16:17], off
	s_nop 0
	global_load_dwordx4 v[158:161], v[20:21], off
	s_nop 0
	global_load_dwordx4 v[20:23], v[178:179], off
	v_add_co_u32_e32 v40, vcc, s6, v24
	s_movk_i32 s6, 0x2000
	s_nop 0
	v_addc_co_u32_e32 v41, vcc, 0, v25, vcc
	v_add_co_u32_e32 v32, vcc, s6, v178
	global_load_dwordx4 v[24:27], v[36:37], off
	global_load_dwordx4 v[28:31], v[40:41], off
	v_addc_co_u32_e32 v33, vcc, 0, v179, vcc
	global_load_dwordx4 v[32:35], v[32:33], off
	s_nop 0
	global_load_dwordx4 v[36:39], v[36:37], off offset:256
	s_nop 0
	global_load_dwordx4 v[40:43], v[40:41], off offset:256
	v_readfirstlane_b32 s75, v0
	s_cmpk_lt_u32 s75, 0x100
	s_waitcnt vmcnt(9)
	ds_write_b128 v192, v[8:11] offset:49152
	s_waitcnt vmcnt(7)
	ds_write_b128 v192, v[16:19] offset:61440
	s_waitcnt vmcnt(5)
	ds_write_b128 v193, v[20:23] offset:49408
	ds_write_b128 v194, v[12:15]
	ds_write_b128 v195, v[4:7]
	s_waitcnt vmcnt(4)
	ds_write_b128 v196, v[24:27]
	s_waitcnt vmcnt(3)
	ds_write_b128 v196, v[28:31] offset:12288
	s_waitcnt vmcnt(2)
	ds_write_b128 v197, v[32:35]
	s_waitcnt vmcnt(1)
	ds_write_b128 v194, v[36:39] offset:16384
	s_waitcnt vmcnt(0)
	ds_write_b128 v195, v[40:43] offset:16384
	s_waitcnt lgkmcnt(0)
	s_barrier
	s_cbranch_scc1 .LBB0_793
	s_waitcnt lgkmcnt(0)
	s_barrier
